# removed the redundant work-group barrier at the head of each SB / NSA unit (the end-of-unit barrier six instructions earlier already orders the work-queue word)
# baseline (speedup 1.0000x reference)
.LBB0_504:
	v_mov_b32_e32 v3, v0
	s_nop 0
	v_cmp_eq_u32_e32 vcc, 0, v3
	s_and_saveexec_b64 s[2:3], vcc
	s_cbranch_execz .LBB0_508
	s_waitcnt vmcnt(4)
	v_mov_b32_e32 v3, v248
	v_mov_b32_e32 v4, s30
	ds_write_b32 v4, v3
	v_mov_b32_e32 v248, 1
	global_atomic_add v248, v2, v248, s[6:7] sc0

.LBB0_561:
	v_mov_b32_e32 v3, v0
	s_nop 0
	v_cmp_eq_u32_e32 vcc, 0, v3
	s_and_saveexec_b64 s[0:1], vcc
	s_cbranch_execz .LBB0_565
	v_readlane_b32 s4, v250, 38
	v_readlane_b32 s5, v250, 39
	s_waitcnt vmcnt(4)
	v_mov_b32_e32 v3, v228
	v_mov_b32_e32 v4, s38
	ds_write_b32 v4, v3
	v_mov_b32_e32 v228, 1
	s_nop 1
	global_atomic_add v228, v2, v228, s[4:5] sc0
